# P13 gather loop: each 16-gather batch is issued only after the previous batch has landed (two waits per token)
# baseline (speedup 1.0000x reference)
.LBB0_1456:
	v_lshl_add_u32 v3, s0, 9, v162
	ds_read2_b32 v[4:5], v3 offset0:64 offset1:68
	ds_read2_b32 v[78:79], v3 offset0:72 offset1:76
	v_mov_b32_e32 v177, 0
	s_waitcnt vmcnt(2)
	v_dot4c_i32_i8_e32 v177, v6, v10
	v_dot4c_i32_i8_e32 v177, v7, v11
	s_waitcnt lgkmcnt(1)
	v_lshl_or_b32 v4, v4, 8, v144
	v_lshl_or_b32 v5, v5, 8, v144
	s_waitcnt vmcnt(0)
	global_load_dwordx4 v[138:141], v4, s[26:27]
	global_load_dwordx4 v[134:137], v5, s[26:27]
	ds_read2_b32 v[4:5], v3 offset0:80 offset1:84
	s_waitcnt lgkmcnt(1)
	v_lshl_or_b32 v78, v78, 8, v144
	v_lshl_or_b32 v79, v79, 8, v144
	global_load_dwordx4 v[130:133], v78, s[26:27]
	global_load_dwordx4 v[122:125], v79, s[26:27]
	ds_read2_b32 v[78:79], v3 offset0:88 offset1:92
	s_waitcnt lgkmcnt(1)
	v_lshl_or_b32 v4, v4, 8, v144
	v_lshl_or_b32 v5, v5, 8, v144
	global_load_dwordx4 v[126:129], v4, s[26:27]
	global_load_dwordx4 v[118:121], v5, s[26:27]
	ds_read2_b32 v[4:5], v3 offset0:96 offset1:100
	s_waitcnt lgkmcnt(1)
	v_lshl_or_b32 v78, v78, 8, v144
	v_lshl_or_b32 v79, v79, 8, v144
	global_load_dwordx4 v[114:117], v78, s[26:27]
	global_load_dwordx4 v[106:109], v79, s[26:27]
	ds_read2_b32 v[78:79], v3 offset0:104 offset1:108
	s_waitcnt lgkmcnt(1)
	v_lshl_or_b32 v4, v4, 8, v144
	v_lshl_or_b32 v5, v5, 8, v144
	global_load_dwordx4 v[110:113], v4, s[26:27]
	global_load_dwordx4 v[102:105], v5, s[26:27]
	ds_read2_b32 v[4:5], v3 offset0:112 offset1:116
	s_waitcnt lgkmcnt(1)
	v_lshl_or_b32 v78, v78, 8, v144
	v_lshl_or_b32 v79, v79, 8, v144
	global_load_dwordx4 v[98:101], v78, s[26:27]
	global_load_dwordx4 v[90:93], v79, s[26:27]
	ds_read2_b32 v[78:79], v3 offset0:120 offset1:124
	s_waitcnt lgkmcnt(1)
	v_lshl_or_b32 v3, v4, 8, v144
	v_lshl_or_b32 v4, v5, 8, v144
	global_load_dwordx4 v[94:97], v3, s[26:27]
	global_load_dwordx4 v[86:89], v4, s[26:27]
	v_dot4c_i32_i8_e32 v177, v8, v12
	s_waitcnt lgkmcnt(0)
	v_lshl_or_b32 v3, v78, 8, v144
	v_lshl_or_b32 v4, v79, 8, v144
	global_load_dwordx4 v[82:85], v3, s[26:27]
	global_load_dwordx4 v[78:81], v4, s[26:27]
	s_waitcnt lgkmcnt(0)
	v_lshl_add_u32 v4, s36, 2, v162
	v_lshl_add_u32 v8, s36, 2, v162
	ds_read_b32 v6, v4
	v_dot4c_i32_i8_e32 v177, v9, v13
	ds_read_b32 v9, v8 offset:240
	ds_read2_b32 v[4:5], v8 offset0:4 offset1:8
	v_mov_b32_e32 v3, 0
	v_mov_b32_e32 v163, 0
	s_waitcnt vmcnt(16)
	v_dot4c_i32_i8_e32 v3, v74, v10
	v_dot4c_i32_i8_e32 v163, v70, v10
	v_dot4c_i32_i8_e32 v3, v75, v11
	v_dot4c_i32_i8_e32 v163, v71, v11
	v_mov_b32_e32 v176, 0
	v_dot4c_i32_i8_e32 v3, v76, v12
	v_dot4c_i32_i8_e32 v163, v72, v12
	v_dot4c_i32_i8_e32 v176, v14, v10
	s_waitcnt lgkmcnt(2)
	v_lshl_or_b32 v14, v6, 8, v144
	ds_read2_b32 v[6:7], v8 offset0:12 offset1:16
	s_waitcnt lgkmcnt(1)
	v_lshl_or_b32 v4, v4, 8, v144
	v_dot4c_i32_i8_e32 v3, v77, v13
	v_dot4c_i32_i8_e32 v163, v73, v13
	s_waitcnt vmcnt(0)
	global_load_dwordx4 v[74:77], v14, s[26:27]
	global_load_dwordx4 v[70:73], v4, s[26:27]
	v_lshl_or_b32 v14, v5, 8, v144
	ds_read2_b32 v[4:5], v8 offset0:20 offset1:24
	v_mov_b32_e32 v164, 0
	v_mov_b32_e32 v165, 0
	v_dot4c_i32_i8_e32 v164, v66, v10
	v_dot4c_i32_i8_e32 v165, v62, v10
	v_mov_b32_e32 v166, 0
	v_mov_b32_e32 v167, 0
	v_dot4c_i32_i8_e32 v164, v67, v11
	v_dot4c_i32_i8_e32 v165, v63, v11
	v_dot4c_i32_i8_e32 v166, v58, v10
	v_dot4c_i32_i8_e32 v167, v54, v10
	v_dot4c_i32_i8_e32 v164, v68, v12
	v_dot4c_i32_i8_e32 v165, v64, v12
	v_dot4c_i32_i8_e32 v166, v59, v11
	v_dot4c_i32_i8_e32 v167, v55, v11
	s_waitcnt lgkmcnt(1)
	v_lshl_or_b32 v6, v6, 8, v144
	v_dot4c_i32_i8_e32 v164, v69, v13
	v_dot4c_i32_i8_e32 v165, v65, v13
	v_dot4c_i32_i8_e32 v166, v60, v12
	v_dot4c_i32_i8_e32 v167, v56, v12
	global_load_dwordx4 v[66:69], v14, s[26:27]
	global_load_dwordx4 v[62:65], v6, s[26:27]
	v_lshl_or_b32 v14, v7, 8, v144
	s_waitcnt lgkmcnt(0)
	v_lshl_or_b32 v4, v4, 8, v144
	ds_read2_b32 v[6:7], v8 offset0:28 offset1:32
	v_dot4c_i32_i8_e32 v166, v61, v13
	v_dot4c_i32_i8_e32 v167, v57, v13
	global_load_dwordx4 v[58:61], v14, s[26:27]
	global_load_dwordx4 v[54:57], v4, s[26:27]
	v_lshl_or_b32 v14, v5, 8, v144
	ds_read2_b32 v[4:5], v8 offset0:36 offset1:40
	v_mov_b32_e32 v168, 0
	v_mov_b32_e32 v169, 0
	v_dot4c_i32_i8_e32 v168, v50, v10
	v_dot4c_i32_i8_e32 v169, v46, v10
	v_mov_b32_e32 v170, 0
	v_mov_b32_e32 v171, 0
	v_dot4c_i32_i8_e32 v168, v51, v11
	v_dot4c_i32_i8_e32 v169, v47, v11
	v_dot4c_i32_i8_e32 v170, v42, v10
	v_dot4c_i32_i8_e32 v171, v38, v10
	v_dot4c_i32_i8_e32 v168, v52, v12
	v_dot4c_i32_i8_e32 v169, v48, v12
	v_dot4c_i32_i8_e32 v170, v43, v11
	v_dot4c_i32_i8_e32 v171, v39, v11
	s_waitcnt lgkmcnt(1)
	v_lshl_or_b32 v6, v6, 8, v144
	v_dot4c_i32_i8_e32 v168, v53, v13
	v_dot4c_i32_i8_e32 v169, v49, v13
	v_dot4c_i32_i8_e32 v170, v44, v12
	v_dot4c_i32_i8_e32 v171, v40, v12
	global_load_dwordx4 v[50:53], v14, s[26:27]
	global_load_dwordx4 v[46:49], v6, s[26:27]
	v_lshl_or_b32 v14, v7, 8, v144
	s_waitcnt lgkmcnt(0)
	v_lshl_or_b32 v4, v4, 8, v144
	ds_read2_b32 v[6:7], v8 offset0:44 offset1:48
	v_dot4c_i32_i8_e32 v170, v45, v13
	v_dot4c_i32_i8_e32 v171, v41, v13
	global_load_dwordx4 v[42:45], v14, s[26:27]
	global_load_dwordx4 v[38:41], v4, s[26:27]
	v_lshl_or_b32 v14, v5, 8, v144
	ds_read2_b32 v[4:5], v8 offset0:52 offset1:56
	v_mov_b32_e32 v172, 0
	v_mov_b32_e32 v173, 0
	v_dot4c_i32_i8_e32 v172, v34, v10
	v_dot4c_i32_i8_e32 v173, v30, v10
	v_mov_b32_e32 v174, 0
	v_mov_b32_e32 v175, 0
	v_dot4c_i32_i8_e32 v172, v35, v11
	v_dot4c_i32_i8_e32 v173, v31, v11
	v_dot4c_i32_i8_e32 v174, v26, v10
	v_dot4c_i32_i8_e32 v175, v22, v10
	v_dot4c_i32_i8_e32 v172, v36, v12
	v_dot4c_i32_i8_e32 v173, v32, v12
	v_dot4c_i32_i8_e32 v174, v27, v11
	v_dot4c_i32_i8_e32 v175, v23, v11
	s_waitcnt lgkmcnt(1)
	v_lshl_or_b32 v6, v6, 8, v144
	v_dot4c_i32_i8_e32 v172, v37, v13
	v_dot4c_i32_i8_e32 v173, v33, v13
	v_dot4c_i32_i8_e32 v174, v28, v12
	v_dot4c_i32_i8_e32 v175, v24, v12
	v_dot4c_i32_i8_e32 v176, v15, v11
	global_load_dwordx4 v[34:37], v14, s[26:27]
	global_load_dwordx4 v[30:33], v6, s[26:27]
	v_lshl_or_b32 v6, v7, 8, v144
	s_waitcnt lgkmcnt(0)
	v_lshl_or_b32 v4, v4, 8, v144
	v_dot4c_i32_i8_e32 v174, v29, v13
	v_dot4c_i32_i8_e32 v175, v25, v13
	v_dot4c_i32_i8_e32 v176, v16, v12
	global_load_dwordx4 v[26:29], v6, s[26:27]
	global_load_dwordx4 v[22:25], v4, s[26:27]
	v_lshl_or_b32 v4, v5, 8, v144
	v_dot4c_i32_i8_e32 v176, v17, v13
	v_lshl_or_b32 v5, v9, 8, v144
	global_load_dwordx4 v[14:17], v4, s[26:27]
	global_load_dwordx4 v[6:9], v5, s[26:27]
	v_mov_b32_e32 v5, 0
	s_waitcnt vmcnt(30)
	v_dot4c_i32_i8_e32 v5, v134, v10
	v_mov_b32_e32 v134, 0
	s_waitcnt vmcnt(29)
	v_dot4c_i32_i8_e32 v134, v130, v10
	v_mov_b32_e32 v130, 0
	s_waitcnt vmcnt(28)
	v_dot4c_i32_i8_e32 v130, v122, v10
	v_dot4c_i32_i8_e32 v130, v123, v11
	v_mov_b32_e32 v123, 0
	s_waitcnt vmcnt(26)
	v_dot4c_i32_i8_e32 v123, v118, v10
	v_mov_b32_e32 v118, 0
	s_waitcnt vmcnt(25)
	v_dot4c_i32_i8_e32 v118, v114, v10
	v_mov_b32_e32 v114, 0
	s_waitcnt vmcnt(24)
	v_dot4c_i32_i8_e32 v114, v106, v10
	v_dot4c_i32_i8_e32 v114, v107, v11
	v_mov_b32_e32 v107, 0
	s_waitcnt vmcnt(22)
	v_dot4c_i32_i8_e32 v107, v102, v10
	v_mov_b32_e32 v102, 0
	v_mov_b32_e32 v4, 0
	s_waitcnt vmcnt(21)
	v_dot4c_i32_i8_e32 v102, v98, v10
	v_mov_b32_e32 v98, 0
	v_dot4c_i32_i8_e32 v4, v138, v10
	s_waitcnt vmcnt(20)
	v_dot4c_i32_i8_e32 v98, v90, v10
	v_dot4c_i32_i8_e32 v4, v139, v11
	v_dot4c_i32_i8_e32 v5, v135, v11
	v_dot4c_i32_i8_e32 v98, v91, v11
	v_mov_b32_e32 v91, 0
	v_dot4c_i32_i8_e32 v4, v140, v12
	v_dot4c_i32_i8_e32 v5, v136, v12
	v_dot4c_i32_i8_e32 v134, v131, v11
	v_mov_b32_e32 v122, 0
	s_waitcnt vmcnt(18)
	v_dot4c_i32_i8_e32 v91, v86, v10
	v_mov_b32_e32 v86, 0
	v_dot4c_i32_i8_e32 v4, v141, v13
	v_dot4c_i32_i8_e32 v5, v137, v13
	v_dot4c_i32_i8_e32 v134, v132, v12
	v_dot4c_i32_i8_e32 v122, v126, v10
	v_mov_b32_e32 v106, 0
	v_mov_b32_e32 v90, 0
	s_waitcnt vmcnt(17)
	v_dot4c_i32_i8_e32 v86, v82, v10
	v_mov_b32_e32 v82, 0
	v_dot4c_i32_i8_e32 v134, v133, v13
	v_dot4c_i32_i8_e32 v130, v124, v12
	v_dot4c_i32_i8_e32 v122, v127, v11
	v_dot4c_i32_i8_e32 v106, v110, v10
	v_dot4c_i32_i8_e32 v90, v94, v10
	s_waitcnt vmcnt(16)
	v_dot4c_i32_i8_e32 v82, v78, v10
	v_cndmask_b32_e64 v10, v3, v4, s[6:7]
	v_cndmask_b32_e64 v3, v4, v3, s[6:7]
	v_cndmask_b32_e64 v4, v163, v5, s[6:7]
	v_cndmask_b32_e64 v5, v5, v163, s[6:7]
	v_dot4c_i32_i8_e32 v130, v125, v13
	v_dot4c_i32_i8_e32 v122, v128, v12
	v_dot4c_i32_i8_e32 v123, v119, v11
	v_add_u32_dpp v3, v10, v3 row_ror:8 row_mask:0xf bank_mask:0xf bound_ctrl:1
	v_add_u32_dpp v4, v4, v5 row_ror:8 row_mask:0xf bank_mask:0xf bound_ctrl:1
	v_cndmask_b32_e64 v5, v164, v134, s[6:7]
	v_cndmask_b32_e64 v10, v134, v164, s[6:7]
	v_dot4c_i32_i8_e32 v122, v129, v13
	v_dot4c_i32_i8_e32 v123, v120, v12
	v_dot4c_i32_i8_e32 v118, v115, v11
	v_dot4c_i32_i8_e32 v106, v111, v11
	v_dot4c_i32_i8_e32 v107, v103, v11
	v_dot4c_i32_i8_e32 v102, v99, v11
	v_dot4c_i32_i8_e32 v90, v95, v11
	v_dot4c_i32_i8_e32 v91, v87, v11
	v_dot4c_i32_i8_e32 v86, v83, v11
	v_dot4c_i32_i8_e32 v82, v79, v11
	v_add_u32_dpp v5, v5, v10 row_ror:8 row_mask:0xf bank_mask:0xf bound_ctrl:1
	v_cndmask_b32_e64 v10, v165, v130, s[6:7]
	v_cndmask_b32_e64 v11, v130, v165, s[6:7]
	v_dot4c_i32_i8_e32 v123, v121, v13
	v_dot4c_i32_i8_e32 v118, v116, v12
	v_dot4c_i32_i8_e32 v114, v108, v12
	v_dot4c_i32_i8_e32 v106, v112, v12
	v_dot4c_i32_i8_e32 v107, v104, v12
	v_dot4c_i32_i8_e32 v102, v100, v12
	v_dot4c_i32_i8_e32 v98, v92, v12
	v_dot4c_i32_i8_e32 v90, v96, v12
	v_dot4c_i32_i8_e32 v91, v88, v12
	v_dot4c_i32_i8_e32 v86, v84, v12
	v_dot4c_i32_i8_e32 v82, v80, v12
	v_add_u32_dpp v10, v10, v11 row_ror:8 row_mask:0xf bank_mask:0xf bound_ctrl:1
	v_cndmask_b32_e64 v11, v166, v122, s[6:7]
	v_cndmask_b32_e64 v12, v122, v166, s[6:7]
	v_dot4c_i32_i8_e32 v118, v117, v13
	v_dot4c_i32_i8_e32 v114, v109, v13
	v_dot4c_i32_i8_e32 v106, v113, v13
	v_dot4c_i32_i8_e32 v107, v105, v13
	v_dot4c_i32_i8_e32 v102, v101, v13
	v_dot4c_i32_i8_e32 v98, v93, v13
	v_dot4c_i32_i8_e32 v90, v97, v13
	v_dot4c_i32_i8_e32 v91, v89, v13
	v_dot4c_i32_i8_e32 v86, v85, v13
	v_dot4c_i32_i8_e32 v82, v81, v13
	v_add_u32_dpp v11, v11, v12 row_ror:8 row_mask:0xf bank_mask:0xf bound_ctrl:1
	v_cndmask_b32_e64 v12, v167, v123, s[6:7]
	v_cndmask_b32_e64 v13, v123, v167, s[6:7]
	v_cndmask_b32_e64 v78, v118, v168, s[6:7]
	v_cndmask_b32_e64 v79, v114, v169, s[6:7]
	v_add_u32_dpp v12, v12, v13 row_ror:8 row_mask:0xf bank_mask:0xf bound_ctrl:1
	v_cndmask_b32_e64 v13, v168, v118, s[6:7]
	v_cndmask_b32_e64 v80, v106, v170, s[6:7]
	v_cndmask_b32_e64 v81, v107, v171, s[6:7]
	v_add_u32_dpp v13, v13, v78 row_ror:8 row_mask:0xf bank_mask:0xf bound_ctrl:1
	v_cndmask_b32_e64 v78, v169, v114, s[6:7]
	v_cndmask_b32_e64 v83, v102, v172, s[6:7]
	v_cndmask_b32_e64 v84, v98, v173, s[6:7]
	v_add_u32_dpp v78, v78, v79 row_ror:8 row_mask:0xf bank_mask:0xf bound_ctrl:1
	v_cndmask_b32_e64 v79, v170, v106, s[6:7]
	v_cndmask_b32_e64 v85, v90, v174, s[6:7]
	v_cndmask_b32_e64 v87, v91, v175, s[6:7]
	v_add_u32_dpp v79, v79, v80 row_ror:8 row_mask:0xf bank_mask:0xf bound_ctrl:1
	v_cndmask_b32_e64 v80, v171, v107, s[6:7]
	s_xor_b32 s0, s0, 1
	v_lshl_add_u64 v[160:161], v[160:161], 0, s[22:23]
	v_add_u32_dpp v80, v80, v81 row_ror:8 row_mask:0xf bank_mask:0xf bound_ctrl:1
	v_cndmask_b32_e64 v81, v172, v102, s[6:7]
	s_andn2_b64 vcc, exec, s[28:29]
	s_mov_b32 s37, s5
	v_add_u32_dpp v81, v81, v83 row_ror:8 row_mask:0xf bank_mask:0xf bound_ctrl:1
	v_cndmask_b32_e64 v83, v173, v98, s[6:7]
	s_nop 1
	v_add_u32_dpp v83, v83, v84 row_ror:8 row_mask:0xf bank_mask:0xf bound_ctrl:1
	v_cndmask_b32_e64 v84, v174, v90, s[6:7]
	s_nop 1
	v_add_u32_dpp v84, v84, v85 row_ror:8 row_mask:0xf bank_mask:0xf bound_ctrl:1
	v_cndmask_b32_e64 v85, v175, v91, s[6:7]
	s_nop 1
	v_add_u32_dpp v85, v85, v87 row_ror:8 row_mask:0xf bank_mask:0xf bound_ctrl:1
	v_cndmask_b32_e64 v87, v176, v86, s[6:7]
	v_cndmask_b32_e64 v86, v86, v176, s[6:7]
	s_nop 1
	v_add_u32_dpp v86, v87, v86 row_ror:8 row_mask:0xf bank_mask:0xf bound_ctrl:1
	v_cndmask_b32_e64 v87, v177, v82, s[6:7]
	v_cndmask_b32_e64 v82, v82, v177, s[6:7]
	s_nop 1
	v_add_u32_dpp v82, v87, v82 row_ror:8 row_mask:0xf bank_mask:0xf bound_ctrl:1
	v_cndmask_b32_e64 v87, v3, v79, s[8:9]
	v_cndmask_b32_e64 v3, v79, v3, s[8:9]
	v_cndmask_b32_e64 v79, v4, v80, s[8:9]
	v_cndmask_b32_e64 v4, v80, v4, s[8:9]
	v_add_u32_dpp v3, v87, v3 row_half_mirror row_mask:0xf bank_mask:0xf bound_ctrl:1
	s_nop 0
	v_add_u32_dpp v4, v79, v4 row_half_mirror row_mask:0xf bank_mask:0xf bound_ctrl:1
	v_cndmask_b32_e64 v79, v5, v81, s[8:9]
	v_cndmask_b32_e64 v5, v81, v5, s[8:9]
	s_nop 1
	v_add_u32_dpp v5, v79, v5 row_half_mirror row_mask:0xf bank_mask:0xf bound_ctrl:1
	v_cndmask_b32_e64 v79, v10, v83, s[8:9]
	v_cndmask_b32_e64 v10, v83, v10, s[8:9]
	s_nop 1
	v_add_u32_dpp v10, v79, v10 row_half_mirror row_mask:0xf bank_mask:0xf bound_ctrl:1
	v_cndmask_b32_e64 v79, v11, v84, s[8:9]
	v_cndmask_b32_e64 v11, v84, v11, s[8:9]
	s_nop 1
	v_add_u32_dpp v11, v79, v11 row_half_mirror row_mask:0xf bank_mask:0xf bound_ctrl:1
	v_cndmask_b32_e64 v79, v12, v85, s[8:9]
	v_cndmask_b32_e64 v12, v85, v12, s[8:9]
	s_nop 1
	v_add_u32_dpp v12, v79, v12 row_half_mirror row_mask:0xf bank_mask:0xf bound_ctrl:1
	v_cndmask_b32_e64 v79, v13, v86, s[8:9]
	v_cndmask_b32_e64 v13, v86, v13, s[8:9]
	s_nop 1
	v_add_u32_dpp v13, v79, v13 row_half_mirror row_mask:0xf bank_mask:0xf bound_ctrl:1
	v_cndmask_b32_e64 v79, v78, v82, s[8:9]
	v_cndmask_b32_e64 v78, v82, v78, s[8:9]
	s_nop 1
	v_add_u32_dpp v78, v79, v78 row_half_mirror row_mask:0xf bank_mask:0xf bound_ctrl:1
	v_cndmask_b32_e64 v79, v3, v11, s[10:11]
	v_cndmask_b32_e64 v3, v11, v3, s[10:11]
	v_cndmask_b32_e64 v11, v4, v12, s[10:11]
	v_cndmask_b32_e64 v4, v12, v4, s[10:11]
	v_add_u32_dpp v3, v79, v3 quad_perm:[2,3,0,1] row_mask:0xf bank_mask:0xf bound_ctrl:1
	s_nop 0
	v_add_u32_dpp v4, v11, v4 quad_perm:[2,3,0,1] row_mask:0xf bank_mask:0xf bound_ctrl:1
	v_cndmask_b32_e64 v11, v5, v13, s[10:11]
	v_cndmask_b32_e64 v5, v13, v5, s[10:11]
	s_nop 1
	v_add_u32_dpp v5, v11, v5 quad_perm:[2,3,0,1] row_mask:0xf bank_mask:0xf bound_ctrl:1
	v_cndmask_b32_e64 v11, v10, v78, s[10:11]
	v_cndmask_b32_e64 v10, v78, v10, s[10:11]
	s_nop 1
	v_add_u32_dpp v10, v11, v10 quad_perm:[2,3,0,1] row_mask:0xf bank_mask:0xf bound_ctrl:1
	v_cndmask_b32_e64 v11, v3, v5, s[12:13]
	v_cndmask_b32_e64 v3, v5, v3, s[12:13]
	v_cndmask_b32_e64 v5, v4, v10, s[12:13]
	v_cndmask_b32_e64 v4, v10, v4, s[12:13]
	v_add_u32_dpp v3, v11, v3 quad_perm:[1,0,3,2] row_mask:0xf bank_mask:0xf bound_ctrl:1
	v_cvt_f32_i32_e32 v3, v3
	v_add_u32_dpp v4, v5, v4 quad_perm:[1,0,3,2] row_mask:0xf bank_mask:0xf bound_ctrl:1
	v_cvt_f32_i32_e32 v4, v4
	v_mov_b64_e32 v[10:11], v[18:19]
	global_store_dword v[158:159], v3, off
	global_store_dword v[158:159], v4, off offset:16
	v_lshl_add_u64 v[158:159], v[158:159], 0, s[20:21]
	v_mov_b64_e32 v[12:13], v[20:21]
	s_cbranch_vccz .LBB0_1450
